# baseline (speedup 1.0000x reference)
.Lrec_stall:
	s_and_b64 vcc, exec, s[8:9]
	s_cbranch_vccnz .Lrec_giveup
	s_add_i32 s43, s43, 1
	s_cmp_lt_u32 s43, s38
	s_cbranch_scc0 .Lrec_dead
	s_and_b64 vcc, exec, s[6:7]
	s_cbranch_vccz .Lrec_noinv
	buffer_inv sc1
.Lrec_noinv:
	s_sleep 2
	s_branch .Lrec_wait
